# gcn layer-2 fast path: per-column-tile epilogue of the recompute MFMA rewritten (bias add in place, cvt_pk then packed f16 max for the relu), 16 VALU instead of 20 per tile and fewer wait states
# speedup vs baseline: 1.0692x; 1.0016x over previous
.LBB5_22:
	s_or_b64 exec, exec, s[14:15]
	v_lshl_or_b32 v74, v74, 6, v109
	global_load_dwordx4 v[74:77], v74, s[10:11]
	s_waitcnt vmcnt(1)
	v_mfma_f32_16x16x32_f16 v[112:115], v[70:73], v[32:35], 0
	v_add_u32_e32 v93, -1, v93
	s_add_i32 s29, s29, 32
	s_add_i32 s28, s28, 2
	v_cmp_eq_u32_e32 vcc, 0, v93
	v_add_u32_e32 v106, 0x100, v106
	s_waitcnt vmcnt(0)
	v_mfma_f32_16x16x32_f16 v[116:119], v[74:77], v[32:35], 0
	s_nop 1
	s_or_b64 s[12:13], vcc, s[12:13]
	s_nop 5
	v_add_f32_e32 v116, v65, v116
	v_add_f32_e32 v117, v65, v117
	v_add_f32_e32 v118, v65, v118
	v_add_f32_e32 v119, v65, v119
	v_add_f32_e32 v112, v65, v112
	v_add_f32_e32 v113, v65, v113
	v_add_f32_e32 v114, v65, v114
	v_add_f32_e32 v115, v65, v115
	v_cvt_pk_f16_f32 v112, v112, v113
	v_cvt_pk_f16_f32 v113, v114, v115
	v_cvt_pk_f16_f32 v114, v116, v117
	v_cvt_pk_f16_f32 v115, v118, v119
	v_pk_max_f16 v112, v112, 0
	v_pk_max_f16 v113, v113, 0
	v_pk_max_f16 v114, v114, 0
	v_pk_max_f16 v115, v115, 0
	v_mfma_f32_16x16x32_f16 v[116:119], v[74:77], v[36:39], 0
	s_nop 0
	v_mfma_f32_16x16x32_f16 v[28:31], v[112:115], v[66:69], v[28:31]
	v_mfma_f32_16x16x32_f16 v[112:115], v[70:73], v[36:39], 0
	s_nop 4
	v_add_f32_e32 v116, v94, v116
	v_add_f32_e32 v117, v94, v117
	v_add_f32_e32 v118, v94, v118
	v_add_f32_e32 v119, v94, v119
	v_add_f32_e32 v112, v94, v112
	v_add_f32_e32 v113, v94, v113
	v_add_f32_e32 v114, v94, v114
	v_add_f32_e32 v115, v94, v115
	v_cvt_pk_f16_f32 v112, v112, v113
	v_cvt_pk_f16_f32 v113, v114, v115
	v_cvt_pk_f16_f32 v114, v116, v117
	v_cvt_pk_f16_f32 v115, v118, v119
	v_pk_max_f16 v112, v112, 0
	v_pk_max_f16 v113, v113, 0
	v_pk_max_f16 v114, v114, 0
	v_pk_max_f16 v115, v115, 0
	v_mfma_f32_16x16x32_f16 v[116:119], v[74:77], v[40:43], 0
	s_nop 0
	v_mfma_f32_16x16x32_f16 v[24:27], v[112:115], v[66:69], v[24:27]
	v_mfma_f32_16x16x32_f16 v[112:115], v[70:73], v[40:43], 0
	s_nop 4
	v_add_f32_e32 v116, v95, v116
	v_add_f32_e32 v117, v95, v117
	v_add_f32_e32 v118, v95, v118
	v_add_f32_e32 v119, v95, v119
	v_add_f32_e32 v112, v95, v112
	v_add_f32_e32 v113, v95, v113
	v_add_f32_e32 v114, v95, v114
	v_add_f32_e32 v115, v95, v115
	v_cvt_pk_f16_f32 v112, v112, v113
	v_cvt_pk_f16_f32 v113, v114, v115
	v_cvt_pk_f16_f32 v114, v116, v117
	v_cvt_pk_f16_f32 v115, v118, v119
	v_pk_max_f16 v112, v112, 0
	v_pk_max_f16 v113, v113, 0
	v_pk_max_f16 v114, v114, 0
	v_pk_max_f16 v115, v115, 0
	v_mfma_f32_16x16x32_f16 v[116:119], v[74:77], v[44:47], 0
	s_nop 0
	v_mfma_f32_16x16x32_f16 v[20:23], v[112:115], v[66:69], v[20:23]
	v_mfma_f32_16x16x32_f16 v[112:115], v[70:73], v[44:47], 0
	s_nop 4
	v_add_f32_e32 v116, v96, v116
	v_add_f32_e32 v117, v96, v117
	v_add_f32_e32 v118, v96, v118
	v_add_f32_e32 v119, v96, v119
	v_add_f32_e32 v112, v96, v112
	v_add_f32_e32 v113, v96, v113
	v_add_f32_e32 v114, v96, v114
	v_add_f32_e32 v115, v96, v115
	v_cvt_pk_f16_f32 v112, v112, v113
	v_cvt_pk_f16_f32 v113, v114, v115
	v_cvt_pk_f16_f32 v114, v116, v117
	v_cvt_pk_f16_f32 v115, v118, v119
	v_pk_max_f16 v112, v112, 0
	v_pk_max_f16 v113, v113, 0
	v_pk_max_f16 v114, v114, 0
	v_pk_max_f16 v115, v115, 0
	v_mfma_f32_16x16x32_f16 v[116:119], v[74:77], v[48:51], 0
	s_nop 0
	v_mfma_f32_16x16x32_f16 v[16:19], v[112:115], v[66:69], v[16:19]
	v_mfma_f32_16x16x32_f16 v[112:115], v[70:73], v[48:51], 0
	s_nop 4
	v_add_f32_e32 v116, v97, v116
	v_add_f32_e32 v117, v97, v117
	v_add_f32_e32 v118, v97, v118
	v_add_f32_e32 v119, v97, v119
	v_add_f32_e32 v112, v97, v112
	v_add_f32_e32 v113, v97, v113
	v_add_f32_e32 v114, v97, v114
	v_add_f32_e32 v115, v97, v115
	v_cvt_pk_f16_f32 v112, v112, v113
	v_cvt_pk_f16_f32 v113, v114, v115
	v_cvt_pk_f16_f32 v114, v116, v117
	v_cvt_pk_f16_f32 v115, v118, v119
	v_pk_max_f16 v112, v112, 0
	v_pk_max_f16 v113, v113, 0
	v_pk_max_f16 v114, v114, 0
	v_pk_max_f16 v115, v115, 0
	v_mfma_f32_16x16x32_f16 v[116:119], v[74:77], v[52:55], 0
	s_nop 0
	v_mfma_f32_16x16x32_f16 v[12:15], v[112:115], v[66:69], v[12:15]
	v_mfma_f32_16x16x32_f16 v[112:115], v[70:73], v[52:55], 0
	s_nop 4
	v_add_f32_e32 v116, v98, v116
	v_add_f32_e32 v117, v98, v117
	v_add_f32_e32 v118, v98, v118
	v_add_f32_e32 v119, v98, v119
	v_add_f32_e32 v112, v98, v112
	v_add_f32_e32 v113, v98, v113
	v_add_f32_e32 v114, v98, v114
	v_add_f32_e32 v115, v98, v115
	v_cvt_pk_f16_f32 v112, v112, v113
	v_cvt_pk_f16_f32 v113, v114, v115
	v_cvt_pk_f16_f32 v114, v116, v117
	v_cvt_pk_f16_f32 v115, v118, v119
	v_pk_max_f16 v112, v112, 0
	v_pk_max_f16 v113, v113, 0
	v_pk_max_f16 v114, v114, 0
	v_pk_max_f16 v115, v115, 0
	v_mfma_f32_16x16x32_f16 v[116:119], v[74:77], v[56:59], 0
	s_nop 0
	v_mfma_f32_16x16x32_f16 v[8:11], v[112:115], v[66:69], v[8:11]
	v_mfma_f32_16x16x32_f16 v[112:115], v[70:73], v[56:59], 0
	s_nop 4
	v_add_f32_e32 v116, v99, v116
	v_add_f32_e32 v117, v99, v117
	v_add_f32_e32 v118, v99, v118
	v_add_f32_e32 v119, v99, v119
	v_add_f32_e32 v112, v99, v112
	v_add_f32_e32 v113, v99, v113
	v_add_f32_e32 v114, v99, v114
	v_add_f32_e32 v115, v99, v115
	v_cvt_pk_f16_f32 v112, v112, v113
	v_cvt_pk_f16_f32 v113, v114, v115
	v_cvt_pk_f16_f32 v114, v116, v117
	v_cvt_pk_f16_f32 v115, v118, v119
	v_pk_max_f16 v112, v112, 0
	v_pk_max_f16 v113, v113, 0
	v_pk_max_f16 v114, v114, 0
	v_pk_max_f16 v115, v115, 0
	v_mfma_f32_16x16x32_f16 v[116:119], v[74:77], v[60:63], 0
	s_nop 0
	v_mfma_f32_16x16x32_f16 v[4:7], v[112:115], v[66:69], v[4:7]
	v_mfma_f32_16x16x32_f16 v[112:115], v[70:73], v[60:63], 0
	s_nop 4
	v_add_f32_e32 v116, v100, v116
	v_add_f32_e32 v117, v100, v117
	v_add_f32_e32 v118, v100, v118
	v_add_f32_e32 v119, v100, v119
	v_add_f32_e32 v112, v100, v112
	v_add_f32_e32 v113, v100, v113
	v_add_f32_e32 v114, v100, v114
	v_add_f32_e32 v115, v100, v115
	v_cvt_pk_f16_f32 v112, v112, v113
	v_cvt_pk_f16_f32 v113, v114, v115
	v_cvt_pk_f16_f32 v114, v116, v117
	v_cvt_pk_f16_f32 v115, v118, v119
	v_pk_max_f16 v112, v112, 0
	v_pk_max_f16 v113, v113, 0
	v_pk_max_f16 v114, v114, 0
	v_pk_max_f16 v115, v115, 0
	s_nop 1
	v_mfma_f32_16x16x32_f16 v[0:3], v[112:115], v[66:69], v[0:3]
	s_andn2_b64 exec, exec, s[12:13]
	s_cbranch_execz .LBB5_43
